# MoE down-GEMM: wave 0 reads the next unit's row-tile counter one K iteration early; a complete early value skips the polling round trip at the hand-off
# speedup vs baseline: 1.0333x; 1.0045x over previous
;     __device__ __forceinline__ bool next(int i, Unit& u) const {
;         const int T = __builtin_amdgcn_readfirstlane(moe[16]), Ng = (T + 7) >> 3, x = c & 7, k = c >> 3; int g;
;         if (TOKEN_ROWS) g = x + 8 * i;
;         else { const int hc = Ng & 7, nl = 8 - hc;
;             if (x >= hc) g = i == 0 ? x - hc : nl + (i - 1) * 8 + (x - hc); else g = 2 * nl + 8 * i + x; }
;         if (g >= Ng) return false;
;         const int rt = g * 8 + (k >> 2); if (rt >= T) return false;
;         u.pn = k & 3; int e = 0;
; #pragma unroll
;         for (int j = 1; j < 16; ++j) e = (rt >= moe[j]) ? j : e;
;         e = __builtin_amdgcn_readfirstlane(e);
;         u.e = e; u.pm = __builtin_amdgcn_readfirstlane(rt - moe[e]); const int left = __builtin_amdgcn_readfirstlane(moe[17 + e]) - u.pm * BM; u.rows = left < BM ? left : BM; return true;
.LBB0_1652:
	v_readlane_b32 s1, v254, 37
	s_add_i32 s62, s62, 1
	s_mov_b64 s[28:29], 0
	v_mov_b32_e32 v0, s1
	ds_read_b32 v0, v0
	s_lshl_b32 s1, s62, 3
	s_add_i32 s5, s1, s33
	s_or_b32 s1, s1, s42
	s_waitcnt lgkmcnt(0)
	v_readfirstlane_b32 s4, v0
	s_add_i32 s6, s4, 7
	s_ashr_i32 s6, s6, 3
	s_and_b32 s7, s6, 7
	s_lshl_b32 s19, s7, 1
	s_cmp_lt_u32 s42, s7
	s_cselect_b32 s1, s5, s1
	s_sub_i32 s1, s1, s19
	s_cmp_ge_i32 s1, s6
	s_cbranch_scc1 .LBB0_1655
	s_lshl_b32 s1, s1, 3
	s_add_i32 s1, s1, s61
	s_mov_b32 s101, s1
	s_cmp_ge_i32 s1, s4
	s_cbranch_scc1 .LBB0_1655
	v_readlane_b32 s4, v254, 38
	s_mov_b64 s[28:29], -1
	s_nop 0
	v_mov_b32_e32 v0, s4
	ds_read2_b32 v[0:1], v0 offset1:1
	v_readlane_b32 s4, v254, 39
	s_waitcnt lgkmcnt(0)
	v_cmp_ge_i32_e32 vcc, s1, v0
	s_nop 1
	v_cndmask_b32_e64 v0, 0, 1, vcc
	v_cmp_lt_i32_e32 vcc, s1, v1
	s_nop 1
	v_cndmask_b32_e32 v2, 2, v0, vcc
	v_mov_b32_e32 v0, s4
	ds_read2_b32 v[0:1], v0 offset1:1
	v_readlane_b32 s4, v254, 40
	s_waitcnt lgkmcnt(0)
	v_cmp_lt_i32_e32 vcc, s1, v0
	s_nop 1
	v_cndmask_b32_e32 v0, 3, v2, vcc
	v_cmp_lt_i32_e32 vcc, s1, v1
	s_nop 1
	v_cndmask_b32_e32 v2, 4, v0, vcc
	v_mov_b32_e32 v0, s4
	ds_read2_b32 v[0:1], v0 offset1:1
	v_readlane_b32 s4, v254, 41
	s_waitcnt lgkmcnt(0)
	v_cmp_lt_i32_e32 vcc, s1, v0
	s_nop 1
	v_cndmask_b32_e32 v0, 5, v2, vcc
	v_cmp_lt_i32_e32 vcc, s1, v1
	s_nop 1
	v_cndmask_b32_e32 v2, 6, v0, vcc
	v_mov_b32_e32 v0, s4
	ds_read2_b32 v[0:1], v0 offset1:1
	v_readlane_b32 s4, v254, 42
	s_waitcnt lgkmcnt(0)
	v_cmp_lt_i32_e32 vcc, s1, v0
	s_nop 1
	v_cndmask_b32_e32 v0, 7, v2, vcc
	v_cmp_lt_i32_e32 vcc, s1, v1
	s_nop 1
	v_cndmask_b32_e32 v2, 8, v0, vcc
	v_mov_b32_e32 v0, s4
	ds_read2_b32 v[0:1], v0 offset1:1
	v_readlane_b32 s4, v254, 43
	s_waitcnt lgkmcnt(0)
	v_cmp_lt_i32_e32 vcc, s1, v0
	s_nop 1
	v_cndmask_b32_e32 v0, 9, v2, vcc
	v_cmp_lt_i32_e32 vcc, s1, v1
	s_nop 1
	v_cndmask_b32_e32 v2, 10, v0, vcc
	v_mov_b32_e32 v0, s4
	ds_read2_b32 v[0:1], v0 offset1:1
	v_readlane_b32 s4, v254, 44
	s_waitcnt lgkmcnt(0)
	v_cmp_lt_i32_e32 vcc, s1, v0
	s_nop 1
	v_cndmask_b32_e32 v0, 11, v2, vcc
	v_cmp_lt_i32_e32 vcc, s1, v1
	s_nop 1
	v_cndmask_b32_e32 v2, 12, v0, vcc
	v_mov_b32_e32 v0, s4
	ds_read2_b32 v[0:1], v0 offset1:1
	v_readlane_b32 s4, v254, 45
	s_waitcnt lgkmcnt(0)
	v_cmp_lt_i32_e32 vcc, s1, v0
	s_nop 1
	v_cndmask_b32_e32 v0, 13, v2, vcc
	v_cmp_lt_i32_e32 vcc, s1, v1
	v_mov_b32_e32 v1, s4
	ds_read_b32 v1, v1
	v_cndmask_b32_e32 v0, 14, v0, vcc
	s_waitcnt lgkmcnt(0)
	v_cmp_lt_i32_e32 vcc, s1, v1
	s_nop 1
	v_cndmask_b32_e32 v0, 15, v0, vcc
	s_nop 0
	v_readfirstlane_b32 s22, v0
	s_lshl_b32 s4, s22, 2
	s_addk_i32 s4, 0x100
	s_add_i32 s4, s4, 0x20040
	v_mov_b32_e32 v0, s4
	ds_read2_b32 v[0:1], v0 offset1:17
	s_waitcnt lgkmcnt(0)
	v_sub_u32_e32 v0, s1, v0
	s_nop 0
	v_readfirstlane_b32 s64, v0
	v_readfirstlane_b32 s1, v1
	s_lshl_b32 s4, s64, 8
	s_sub_i32 s1, s1, s4
	s_min_i32 s65, s1, 0x100

; __device__ __forceinline__ int lane_id() { int l; asm volatile("v_mbcnt_lo_u32_b32 %0, -1, 0\n\tv_mbcnt_hi_u32_b32 %0, -1, %0" : "=v"(l)); return l; }
;     __device__ __forceinline__ void a_ready(const Unit& u, int wv) const { if (wready) wait_counter(wready + 64 * u.pm, wneed, wtmo, wv); }
;     __device__ __forceinline__ void a_ready(const Unit& u, const int wv) const {
;         if (!TOKEN_ROWS) {
;             if (wv == 0) {
;                 const unsigned* w = ready + 64 * (moe[u.e] + u.pm); const unsigned long long t0 = __builtin_amdgcn_s_memrealtime(); unsigned polls = 0;
;                 while ((unsigned)__builtin_amdgcn_readfirstlane(__hip_atomic_load(w, __ATOMIC_RELAXED, __HIP_MEMORY_SCOPE_AGENT)) < 32u) {
;                     if ((++polls & 255u) == 0u && __builtin_amdgcn_readfirstlane(__hip_atomic_load(tmo, __ATOMIC_RELAXED, __HIP_MEMORY_SCOPE_AGENT)) != 0u) break;
;                     if (__builtin_amdgcn_s_memrealtime() - t0 > 2000000ull) { if (lane_id() == 0) __hip_atomic_store(tmo, 1u, __ATOMIC_RELAXED, __HIP_MEMORY_SCOPE_AGENT); break; }
;                     __builtin_amdgcn_s_sleep(2); }
;     ...
;             const bool last = (t == nt - 2);
;             const char* a1 = cA0 + (size_t)(t + 1) * kstep;
;             const char* a2 = last ? nA0 : cA0 + (size_t)(t + 2) * kstep; const char* b2 = last ? nB : cB + (size_t)(t + 2) * kstep;
;             const char* a3 = a2 + kstep; const char* b3 = b2 + kstep;
;             unsigned p0[2], p1[2];
; #pragma unroll
;             for (int i = 0; i < 2; ++i) { p0[i] = DN ? voffA[i] : (last ? oN0[i] : oA0[i]); p1[i] = DN ? voffA[i] : (last ? oN1[i] : oA1[i]); }
;             if (last && has_next) S.a_ready(nxt, wv);
.LBB0_1662:
	s_cmp_eq_u32 s68, 4
	s_cbranch_scc0 .Lm2ep_skip
	s_and_b64 vcc, exec, s[78:79]
	s_cbranch_vccnz .Lm2ep_skip
	s_andn2_b64 vcc, exec, s[28:29]
	s_cbranch_vccnz .Lm2ep_skip
	s_lshl_b32 s30, s101, 8
	s_add_u32 s30, s43, s30
	s_addc_u32 s31, s44, 0
	global_load_dword v234, v65, s[30:31] sc1
.Lm2ep_skip:
	s_cmp_eq_u32 s68, 6
	s_cselect_b64 s[6:7], -1, 0
	s_and_b64 s[30:31], s[28:29], s[6:7]
	s_andn2_b64 vcc, exec, s[30:31]
	s_cbranch_vccnz .LBB0_1661
	s_and_b64 vcc, exec, s[78:79]
	s_cbranch_vccnz .LBB0_1660
	v_readfirstlane_b32 s30, v234
	s_cmp_gt_u32 s30, 31
	s_cbranch_scc1 .LBB0_1660
	v_mov_b32_e32 v64, s23
	ds_read_b32 v64, v64
	s_memrealtime s[34:35]
	s_mov_b32 s69, 1
	s_waitcnt lgkmcnt(0)
	v_readfirstlane_b32 s30, v64
	s_add_i32 s30, s30, s64
	s_lshl_b32 s30, s30, 6
	s_ashr_i32 s31, s30, 31
	s_lshl_b64 s[30:31], s[30:31], 2
	s_add_u32 s30, s43, s30
	s_addc_u32 s31, s44, s31
	s_branch .LBB0_1667
